# C1 + grid barriers: waiting workgroups invalidate only L1 (buffer_inv sc0); the XCD's last arriver already invalidated the shared L2 before releasing them
# speedup vs baseline: 1.0196x; 1.0161x over previous
.LBB0_76:
	s_or_b64 exec, exec, s[10:11]
	s_waitcnt vmcnt(0)
	buffer_inv sc0
	s_waitcnt vmcnt(0)

.LBB0_171:
	s_or_b64 exec, exec, s[12:13]
	s_waitcnt vmcnt(0)
	buffer_inv sc0
	s_waitcnt vmcnt(0)

.LBB0_1445:
	s_or_b64 exec, exec, s[30:31]
	s_waitcnt vmcnt(0)
	buffer_inv sc0
	s_waitcnt vmcnt(0)

.LBB0_1695:
	s_or_b64 exec, exec, s[8:9]
	s_waitcnt vmcnt(0)
	buffer_inv sc0
	s_waitcnt vmcnt(0)
